# gate-up GEMM epilogue (SwiGLU): packed multiplies, transcendentals interleaved with the packed ops
# speedup vs baseline: 1.0113x; 1.0113x over previous
; __device__ __forceinline__ unsigned pk4_fp8(float a, float b, float c, float d) { int w = 0; w = __builtin_amdgcn_cvt_pk_fp8_f32(a, b, w, false); w = __builtin_amdgcn_cvt_pk_fp8_f32(c, d, w, true); return (unsigned)w; }
; __device__ __forceinline__ float silu_mul(float g, float u) { const float e = __builtin_amdgcn_exp2f(g * -1.4426950408889634f); return g * __builtin_amdgcn_rcpf(1.0f + e) * u; }
;     __device__ __forceinline__ void operator()(const f32x4 (&acc)[2][2][4][2], const Unit& u, int wr, int wc, int fr, int fq) const {
;     ...
;         const int row0 = u.pm * BM + wr * 64 + fr, col0 = u.pn * HALF + wc * 32 + 8 * fq;
; #pragma unroll
;         for (int ai = 0; ai < 2; ++ai)
; #pragma unroll
;             for (int m = 0; m < 4; ++m) { unsigned char* rowp = O + (size_t)(row0 + ai * HALF + m * 16) * ldc + col0;
;                 const f32x4 g0 = acc[ai][0][m][0], g1 = acc[ai][0][m][1], u0 = acc[ai][1][m][0], u1 = acc[ai][1][m][1];
;                 u32x2 w; w.x = pk4_fp8(silu_mul(g0[0], u0[0]), silu_mul(g0[1], u0[1]), silu_mul(g0[2], u0[2]), silu_mul(g0[3], u0[3]));
;                 w.y = pk4_fp8(silu_mul(g1[0], u1[0]), silu_mul(g1[1], u1[1]), silu_mul(g1[2], u1[2]), silu_mul(g1[3], u1[3]));
;                 *(u32x2*)rowp = w; }
.LBB0_1852:
	s_lshl_b32 s15, s42, 8
	v_readlane_b32 s18, v252, 1
	v_mbcnt_lo_u32_b32 v66, -1, 0
	v_mbcnt_hi_u32_b32 v66, -1, v66
	s_add_i32 s15, s15, s18
	v_and_or_b32 v0, v66, 15, s15
	s_lshl_b32 s15, s34, 7
	v_ashrrev_i32_e32 v66, 1, v66
	s_or_b32 s15, s15, s77
	v_and_b32_e32 v66, -8, v66
	v_add_u32_e32 v130, s15, v66
	s_mov_b32 s98, 0xbfb8aa3b
	v_pk_mul_f32 v[66:67], v[126:127], s[98:99] op_sel_hi:[1,0]
	v_pk_mul_f32 v[68:69], v[128:129], s[98:99] op_sel_hi:[1,0]
	v_exp_f32_e32 v66, v66
	v_exp_f32_e32 v67, v67
	v_pk_mul_f32 v[74:75], v[118:119], s[98:99] op_sel_hi:[1,0]
	v_exp_f32_e32 v68, v68
	v_exp_f32_e32 v69, v69
	v_pk_mul_f32 v[76:77], v[120:121], s[98:99] op_sel_hi:[1,0]
	v_add_f32_e32 v66, 1.0, v66
	v_exp_f32_e32 v74, v74
	v_add_f32_e32 v67, 1.0, v67
	v_exp_f32_e32 v75, v75
	v_add_f32_e32 v68, 1.0, v68
	v_exp_f32_e32 v76, v76
	v_add_f32_e32 v69, 1.0, v69
	v_exp_f32_e32 v77, v77
	v_rcp_f32_e32 v66, v66
	v_add_f32_e32 v74, 1.0, v74
	v_rcp_f32_e32 v67, v67
	v_add_f32_e32 v75, 1.0, v75
	v_rcp_f32_e32 v68, v68
	v_add_f32_e32 v76, 1.0, v76
	v_rcp_f32_e32 v69, v69
	v_add_f32_e32 v77, 1.0, v77
	v_pk_mul_f32 v[66:67], v[126:127], v[66:67]
	v_rcp_f32_e32 v74, v74
	v_pk_mul_f32 v[68:69], v[128:129], v[68:69]
	v_rcp_f32_e32 v75, v75
	v_pk_mul_f32 v[66:67], v[122:123], v[66:67]
	v_rcp_f32_e32 v76, v76
	v_pk_mul_f32 v[68:69], v[124:125], v[68:69]
	v_rcp_f32_e32 v77, v77
	v_pk_mul_f32 v[74:75], v[118:119], v[74:75]
	v_pk_mul_f32 v[74:75], v[114:115], v[74:75]
	v_pk_mul_f32 v[76:77], v[120:121], v[76:77]
	v_pk_mul_f32 v[76:77], v[116:117], v[76:77]
	v_cvt_pk_fp8_f32 v66, v66, v67
	v_cvt_pk_fp8_f32 v66, v68, v69 op_sel:[0,0,1]
	v_cvt_pk_fp8_f32 v67, v74, v75
	v_cvt_pk_fp8_f32 v67, v76, v77 op_sel:[0,0,1]
	v_mov_b64_e32 v[132:133], s[0:1]
	v_ashrrev_i32_e32 v131, 31, v130
	v_mad_i64_i32 v[68:69], s[18:19], v0, s78, v[132:133]
	v_lshl_add_u64 v[68:69], v[68:69], 0, v[130:131]
	global_store_dwordx2 v[68:69], v[66:67], off
	v_pk_mul_f32 v[66:67], v[110:111], s[98:99] op_sel_hi:[1,0]
	v_pk_mul_f32 v[68:69], v[112:113], s[98:99] op_sel_hi:[1,0]
	v_exp_f32_e32 v66, v66
	v_exp_f32_e32 v67, v67
	v_pk_mul_f32 v[74:75], v[102:103], s[98:99] op_sel_hi:[1,0]
	v_exp_f32_e32 v68, v68
	v_exp_f32_e32 v69, v69
	v_pk_mul_f32 v[76:77], v[104:105], s[98:99] op_sel_hi:[1,0]
	v_add_f32_e32 v66, 1.0, v66
	v_exp_f32_e32 v74, v74
	v_add_f32_e32 v67, 1.0, v67
	v_exp_f32_e32 v75, v75
	v_add_f32_e32 v68, 1.0, v68
	v_exp_f32_e32 v76, v76
	v_add_f32_e32 v69, 1.0, v69
	v_exp_f32_e32 v77, v77
	v_rcp_f32_e32 v66, v66
	v_add_f32_e32 v74, 1.0, v74
	v_rcp_f32_e32 v67, v67
	v_add_f32_e32 v75, 1.0, v75
	v_rcp_f32_e32 v68, v68
	v_add_f32_e32 v76, 1.0, v76
	v_rcp_f32_e32 v69, v69
	v_add_f32_e32 v77, 1.0, v77
	v_pk_mul_f32 v[66:67], v[110:111], v[66:67]
	v_rcp_f32_e32 v74, v74
	v_pk_mul_f32 v[68:69], v[112:113], v[68:69]
	v_rcp_f32_e32 v75, v75
	v_pk_mul_f32 v[66:67], v[106:107], v[66:67]
	v_rcp_f32_e32 v76, v76
	v_pk_mul_f32 v[68:69], v[108:109], v[68:69]
	v_rcp_f32_e32 v77, v77
	v_pk_mul_f32 v[74:75], v[102:103], v[74:75]
	v_pk_mul_f32 v[74:75], v[98:99], v[74:75]
	v_pk_mul_f32 v[76:77], v[104:105], v[76:77]
	v_pk_mul_f32 v[76:77], v[100:101], v[76:77]
	v_cvt_pk_fp8_f32 v66, v66, v67
	v_cvt_pk_fp8_f32 v66, v68, v69 op_sel:[0,0,1]
	v_cvt_pk_fp8_f32 v67, v74, v75
	v_cvt_pk_fp8_f32 v67, v76, v77 op_sel:[0,0,1]
	v_or_b32_e32 v68, 16, v0
	v_mad_i64_i32 v[68:69], s[18:19], v68, s78, v[132:133]
	v_lshl_add_u64 v[68:69], v[68:69], 0, v[130:131]
	global_store_dwordx2 v[68:69], v[66:67], off
	v_pk_mul_f32 v[66:67], v[94:95], s[98:99] op_sel_hi:[1,0]
	v_pk_mul_f32 v[68:69], v[96:97], s[98:99] op_sel_hi:[1,0]
	v_exp_f32_e32 v66, v66
	v_exp_f32_e32 v67, v67
	v_pk_mul_f32 v[74:75], v[86:87], s[98:99] op_sel_hi:[1,0]
	v_exp_f32_e32 v68, v68
	v_exp_f32_e32 v69, v69
	v_pk_mul_f32 v[76:77], v[88:89], s[98:99] op_sel_hi:[1,0]
	v_add_f32_e32 v66, 1.0, v66
	v_exp_f32_e32 v74, v74
	v_add_f32_e32 v67, 1.0, v67
	v_exp_f32_e32 v75, v75
	v_add_f32_e32 v68, 1.0, v68
	v_exp_f32_e32 v76, v76
	v_add_f32_e32 v69, 1.0, v69
	v_exp_f32_e32 v77, v77
	v_rcp_f32_e32 v66, v66
	v_add_f32_e32 v74, 1.0, v74
	v_rcp_f32_e32 v67, v67
	v_add_f32_e32 v75, 1.0, v75
	v_rcp_f32_e32 v68, v68
	v_add_f32_e32 v76, 1.0, v76
	v_rcp_f32_e32 v69, v69
	v_add_f32_e32 v77, 1.0, v77
	v_pk_mul_f32 v[66:67], v[94:95], v[66:67]
	v_rcp_f32_e32 v74, v74
	v_pk_mul_f32 v[68:69], v[96:97], v[68:69]
	v_rcp_f32_e32 v75, v75
	v_pk_mul_f32 v[66:67], v[90:91], v[66:67]
	v_rcp_f32_e32 v76, v76
	v_pk_mul_f32 v[68:69], v[92:93], v[68:69]
	v_rcp_f32_e32 v77, v77
	v_pk_mul_f32 v[74:75], v[86:87], v[74:75]
	v_pk_mul_f32 v[74:75], v[82:83], v[74:75]
	v_pk_mul_f32 v[76:77], v[88:89], v[76:77]
	v_pk_mul_f32 v[76:77], v[84:85], v[76:77]
	v_cvt_pk_fp8_f32 v66, v66, v67
	v_cvt_pk_fp8_f32 v66, v68, v69 op_sel:[0,0,1]
	v_cvt_pk_fp8_f32 v67, v74, v75
	v_cvt_pk_fp8_f32 v67, v76, v77 op_sel:[0,0,1]
	v_or_b32_e32 v68, 32, v0
	v_mad_i64_i32 v[68:69], s[18:19], v68, s78, v[132:133]
	v_lshl_add_u64 v[68:69], v[68:69], 0, v[130:131]
	global_store_dwordx2 v[68:69], v[66:67], off
	v_pk_mul_f32 v[66:67], v[78:79], s[98:99] op_sel_hi:[1,0]
	v_pk_mul_f32 v[68:69], v[80:81], s[98:99] op_sel_hi:[1,0]
	v_exp_f32_e32 v66, v66
	v_exp_f32_e32 v67, v67
	v_pk_mul_f32 v[74:75], v[70:71], s[98:99] op_sel_hi:[1,0]
	v_exp_f32_e32 v68, v68
	v_exp_f32_e32 v69, v69
	v_pk_mul_f32 v[76:77], v[72:73], s[98:99] op_sel_hi:[1,0]
	v_add_f32_e32 v66, 1.0, v66
	v_exp_f32_e32 v74, v74
	v_add_f32_e32 v67, 1.0, v67
	v_exp_f32_e32 v75, v75
	v_add_f32_e32 v68, 1.0, v68
	v_exp_f32_e32 v76, v76
	v_add_f32_e32 v69, 1.0, v69
	v_exp_f32_e32 v77, v77
	v_rcp_f32_e32 v66, v66
	v_add_f32_e32 v74, 1.0, v74
; __device__ __forceinline__ unsigned pk4_fp8(float a, float b, float c, float d) { int w = 0; w = __builtin_amdgcn_cvt_pk_fp8_f32(a, b, w, false); w = __builtin_amdgcn_cvt_pk_fp8_f32(c, d, w, true); return (unsigned)w; }
; __device__ __forceinline__ float silu_mul(float g, float u) { const float e = __builtin_amdgcn_exp2f(g * -1.4426950408889634f); return g * __builtin_amdgcn_rcpf(1.0f + e) * u; }
;     __device__ __forceinline__ void operator()(const f32x4 (&acc)[2][2][4][2], const Unit& u, int wr, int wc, int fr, int fq) const {
;     ...
;         const int row0 = u.pm * BM + wr * 64 + fr, col0 = u.pn * HALF + wc * 32 + 8 * fq;
; #pragma unroll
;         for (int ai = 0; ai < 2; ++ai)
; #pragma unroll
;             for (int m = 0; m < 4; ++m) { unsigned char* rowp = O + (size_t)(row0 + ai * HALF + m * 16) * ldc + col0;
;                 const f32x4 g0 = acc[ai][0][m][0], g1 = acc[ai][0][m][1], u0 = acc[ai][1][m][0], u1 = acc[ai][1][m][1];
;                 u32x2 w; w.x = pk4_fp8(silu_mul(g0[0], u0[0]), silu_mul(g0[1], u0[1]), silu_mul(g0[2], u0[2]), silu_mul(g0[3], u0[3]));
;                 w.y = pk4_fp8(silu_mul(g1[0], u1[0]), silu_mul(g1[1], u1[1]), silu_mul(g1[2], u1[2]), silu_mul(g1[3], u1[3]));
;                 *(u32x2*)rowp = w; }
	v_rcp_f32_e32 v67, v67
	v_add_f32_e32 v75, 1.0, v75
	v_rcp_f32_e32 v68, v68
	v_add_f32_e32 v76, 1.0, v76
	v_rcp_f32_e32 v69, v69
	v_add_f32_e32 v77, 1.0, v77
	v_pk_mul_f32 v[66:67], v[78:79], v[66:67]
	v_rcp_f32_e32 v74, v74
	v_pk_mul_f32 v[68:69], v[80:81], v[68:69]
	v_rcp_f32_e32 v75, v75
	v_pk_mul_f32 v[66:67], v[194:195], v[66:67]
	v_rcp_f32_e32 v76, v76
	v_pk_mul_f32 v[68:69], v[196:197], v[68:69]
	v_rcp_f32_e32 v77, v77
	v_pk_mul_f32 v[74:75], v[70:71], v[74:75]
	v_pk_mul_f32 v[74:75], v[204:205], v[74:75]
	v_pk_mul_f32 v[76:77], v[72:73], v[76:77]
	v_pk_mul_f32 v[76:77], v[206:207], v[76:77]
	v_cvt_pk_fp8_f32 v66, v66, v67
	v_cvt_pk_fp8_f32 v66, v68, v69 op_sel:[0,0,1]
	v_cvt_pk_fp8_f32 v67, v74, v75
	v_cvt_pk_fp8_f32 v67, v76, v77 op_sel:[0,0,1]
	v_or_b32_e32 v68, 48, v0
	v_mad_i64_i32 v[68:69], s[18:19], v68, s78, v[132:133]
	v_lshl_add_u64 v[68:69], v[68:69], 0, v[130:131]
	global_store_dwordx2 v[68:69], v[66:67], off
	v_pk_mul_f32 v[66:67], v[62:63], s[98:99] op_sel_hi:[1,0]
	v_pk_mul_f32 v[68:69], v[64:65], s[98:99] op_sel_hi:[1,0]
	v_exp_f32_e32 v66, v66
	v_exp_f32_e32 v67, v67
	v_pk_mul_f32 v[74:75], v[54:55], s[98:99] op_sel_hi:[1,0]
	v_exp_f32_e32 v68, v68
	v_exp_f32_e32 v69, v69
	v_pk_mul_f32 v[76:77], v[56:57], s[98:99] op_sel_hi:[1,0]
	v_add_f32_e32 v66, 1.0, v66
	v_exp_f32_e32 v74, v74
	v_add_f32_e32 v67, 1.0, v67
	v_exp_f32_e32 v75, v75
	v_add_f32_e32 v68, 1.0, v68
	v_exp_f32_e32 v76, v76
	v_add_f32_e32 v69, 1.0, v69
	v_exp_f32_e32 v77, v77
	v_rcp_f32_e32 v66, v66
	v_add_f32_e32 v74, 1.0, v74
	v_rcp_f32_e32 v67, v67
	v_add_f32_e32 v75, 1.0, v75
	v_rcp_f32_e32 v68, v68
	v_add_f32_e32 v76, 1.0, v76
	v_rcp_f32_e32 v69, v69
	v_add_f32_e32 v77, 1.0, v77
	v_pk_mul_f32 v[66:67], v[62:63], v[66:67]
	v_rcp_f32_e32 v74, v74
	v_pk_mul_f32 v[68:69], v[64:65], v[68:69]
	v_rcp_f32_e32 v75, v75
	v_pk_mul_f32 v[66:67], v[58:59], v[66:67]
	v_rcp_f32_e32 v76, v76
	v_pk_mul_f32 v[68:69], v[60:61], v[68:69]
	v_rcp_f32_e32 v77, v77
	v_pk_mul_f32 v[74:75], v[54:55], v[74:75]
	v_pk_mul_f32 v[74:75], v[50:51], v[74:75]
	v_pk_mul_f32 v[76:77], v[56:57], v[76:77]
	v_pk_mul_f32 v[76:77], v[52:53], v[76:77]
	v_cvt_pk_fp8_f32 v58, v66, v67
	v_cvt_pk_fp8_f32 v58, v68, v69 op_sel:[0,0,1]
	v_cvt_pk_fp8_f32 v59, v74, v75
	v_cvt_pk_fp8_f32 v59, v76, v77 op_sel:[0,0,1]
	v_add_u32_e32 v68, 0x80, v0
	s_andn2_b64 vcc, exec, s[40:41]
	v_mad_i64_i32 v[50:51], s[18:19], v68, s78, v[132:133]
	v_lshl_add_u64 v[50:51], v[50:51], 0, v[130:131]
	global_store_dwordx2 v[50:51], v[58:59], off
	v_pk_mul_f32 v[66:67], v[46:47], s[98:99] op_sel_hi:[1,0]
	v_pk_mul_f32 v[68:69], v[48:49], s[98:99] op_sel_hi:[1,0]
	v_exp_f32_e32 v66, v66
	v_exp_f32_e32 v67, v67
	v_pk_mul_f32 v[74:75], v[38:39], s[98:99] op_sel_hi:[1,0]
	v_exp_f32_e32 v68, v68
	v_exp_f32_e32 v69, v69
	v_pk_mul_f32 v[76:77], v[40:41], s[98:99] op_sel_hi:[1,0]
	v_add_f32_e32 v66, 1.0, v66
	v_exp_f32_e32 v74, v74
	v_add_f32_e32 v67, 1.0, v67
	v_exp_f32_e32 v75, v75
	v_add_f32_e32 v68, 1.0, v68
	v_exp_f32_e32 v76, v76
	v_add_f32_e32 v69, 1.0, v69
	v_exp_f32_e32 v77, v77
	v_rcp_f32_e32 v66, v66
	v_add_f32_e32 v74, 1.0, v74
	v_rcp_f32_e32 v67, v67
	v_add_f32_e32 v75, 1.0, v75
	v_rcp_f32_e32 v68, v68
	v_add_f32_e32 v76, 1.0, v76
	v_rcp_f32_e32 v69, v69
	v_add_f32_e32 v77, 1.0, v77
	v_pk_mul_f32 v[66:67], v[46:47], v[66:67]
	v_rcp_f32_e32 v74, v74
	v_pk_mul_f32 v[68:69], v[48:49], v[68:69]
	v_rcp_f32_e32 v75, v75
	v_pk_mul_f32 v[66:67], v[42:43], v[66:67]
	v_rcp_f32_e32 v76, v76
	v_pk_mul_f32 v[68:69], v[44:45], v[68:69]
	v_rcp_f32_e32 v77, v77
	v_pk_mul_f32 v[74:75], v[38:39], v[74:75]
	v_pk_mul_f32 v[74:75], v[34:35], v[74:75]
; __device__ __forceinline__ int lane_id() { int l; asm volatile("v_mbcnt_lo_u32_b32 %0, -1, 0\n\tv_mbcnt_hi_u32_b32 %0, -1, %0" : "=v"(l)); return l; }
; __device__ __forceinline__ unsigned pk4_fp8(float a, float b, float c, float d) { int w = 0; w = __builtin_amdgcn_cvt_pk_fp8_f32(a, b, w, false); w = __builtin_amdgcn_cvt_pk_fp8_f32(c, d, w, true); return (unsigned)w; }
; __device__ __forceinline__ float silu_mul(float g, float u) { const float e = __builtin_amdgcn_exp2f(g * -1.4426950408889634f); return g * __builtin_amdgcn_rcpf(1.0f + e) * u; }
; #define PG8_BAR __builtin_amdgcn_s_barrier()
;     __device__ __forceinline__ void operator()(const f32x4 (&acc)[2][2][4][2], const Unit& u, int wr, int wc, int fr, int fq) const {
;     ...
;         const int row0 = u.pm * BM + wr * 64 + fr, col0 = u.pn * HALF + wc * 32 + 8 * fq;
; #pragma unroll
;         for (int ai = 0; ai < 2; ++ai)
; #pragma unroll
;             for (int m = 0; m < 4; ++m) { unsigned char* rowp = O + (size_t)(row0 + ai * HALF + m * 16) * ldc + col0;
;                 const f32x4 g0 = acc[ai][0][m][0], g1 = acc[ai][0][m][1], u0 = acc[ai][1][m][0], u1 = acc[ai][1][m][1];
;                 u32x2 w; w.x = pk4_fp8(silu_mul(g0[0], u0[0]), silu_mul(g0[1], u0[1]), silu_mul(g0[2], u0[2]), silu_mul(g0[3], u0[3]));
;                 w.y = pk4_fp8(silu_mul(g1[0], u1[0]), silu_mul(g1[1], u1[1]), silu_mul(g1[2], u1[2]), silu_mul(g1[3], u1[3]));
;                 *(u32x2*)rowp = w; }
; template <class Epi, class Sched, bool ALIGN_EPI = false, bool SP2 = false, bool FP8 = false>
; __device__ __forceinline__ void gemm_phase(PG8_LAS unsigned char* lds, const Gemm g, const Sched& S, const Epi& E, const int wave_) {
;     ...
;         if constexpr (ALIGN_EPI) { if (wr == 0) PG8_BAR; }
;         if constexpr (!Epi::AFTER_DRAIN) { const int l2_ = lane_id(); E(acc, cur, wr, wc, l2_ & 15, l2_ >> 4); S.done(cur); }
;         if (!has_next) break;
	v_pk_mul_f32 v[76:77], v[40:41], v[76:77]
	v_pk_mul_f32 v[76:77], v[36:37], v[76:77]
	v_cvt_pk_fp8_f32 v42, v66, v67
	v_cvt_pk_fp8_f32 v42, v68, v69 op_sel:[0,0,1]
	v_cvt_pk_fp8_f32 v43, v74, v75
	v_cvt_pk_fp8_f32 v43, v76, v77 op_sel:[0,0,1]
	v_add_u32_e32 v52, 0x90, v0
	v_mad_i64_i32 v[34:35], s[18:19], v52, s78, v[132:133]
	v_lshl_add_u64 v[34:35], v[34:35], 0, v[130:131]
	global_store_dwordx2 v[34:35], v[42:43], off
	v_pk_mul_f32 v[66:67], v[30:31], s[98:99] op_sel_hi:[1,0]
	v_pk_mul_f32 v[68:69], v[32:33], s[98:99] op_sel_hi:[1,0]
	v_exp_f32_e32 v66, v66
	v_exp_f32_e32 v67, v67
	v_pk_mul_f32 v[74:75], v[22:23], s[98:99] op_sel_hi:[1,0]
	v_exp_f32_e32 v68, v68
	v_exp_f32_e32 v69, v69
	v_pk_mul_f32 v[76:77], v[24:25], s[98:99] op_sel_hi:[1,0]
	v_add_f32_e32 v66, 1.0, v66
	v_exp_f32_e32 v74, v74
	v_add_f32_e32 v67, 1.0, v67
	v_exp_f32_e32 v75, v75
	v_add_f32_e32 v68, 1.0, v68
	v_exp_f32_e32 v76, v76
	v_add_f32_e32 v69, 1.0, v69
	v_exp_f32_e32 v77, v77
	v_rcp_f32_e32 v66, v66
	v_add_f32_e32 v74, 1.0, v74
	v_rcp_f32_e32 v67, v67
	v_add_f32_e32 v75, 1.0, v75
	v_rcp_f32_e32 v68, v68
	v_add_f32_e32 v76, 1.0, v76
	v_rcp_f32_e32 v69, v69
	v_add_f32_e32 v77, 1.0, v77
	v_pk_mul_f32 v[66:67], v[30:31], v[66:67]
	v_rcp_f32_e32 v74, v74
	v_pk_mul_f32 v[68:69], v[32:33], v[68:69]
	v_rcp_f32_e32 v75, v75
	v_pk_mul_f32 v[66:67], v[26:27], v[66:67]
	v_rcp_f32_e32 v76, v76
	v_pk_mul_f32 v[68:69], v[28:29], v[68:69]
	v_rcp_f32_e32 v77, v77
	v_pk_mul_f32 v[74:75], v[22:23], v[74:75]
	v_pk_mul_f32 v[74:75], v[18:19], v[74:75]
	v_pk_mul_f32 v[76:77], v[24:25], v[76:77]
	v_pk_mul_f32 v[76:77], v[20:21], v[76:77]
	v_cvt_pk_fp8_f32 v26, v66, v67
	v_cvt_pk_fp8_f32 v26, v68, v69 op_sel:[0,0,1]
	v_cvt_pk_fp8_f32 v27, v74, v75
	v_cvt_pk_fp8_f32 v27, v76, v77 op_sel:[0,0,1]
	v_add_u32_e32 v36, 0xa0, v0
	v_add_u32_e32 v0, 0xb0, v0
	v_mad_i64_i32 v[18:19], s[18:19], v36, s78, v[132:133]
	v_lshl_add_u64 v[18:19], v[18:19], 0, v[130:131]
	global_store_dwordx2 v[18:19], v[26:27], off
	v_pk_mul_f32 v[66:67], v[14:15], s[98:99] op_sel_hi:[1,0]
	v_pk_mul_f32 v[68:69], v[16:17], s[98:99] op_sel_hi:[1,0]
	v_exp_f32_e32 v66, v66
	v_exp_f32_e32 v67, v67
	v_pk_mul_f32 v[74:75], v[6:7], s[98:99] op_sel_hi:[1,0]
	v_exp_f32_e32 v68, v68
	v_exp_f32_e32 v69, v69
	v_pk_mul_f32 v[76:77], v[8:9], s[98:99] op_sel_hi:[1,0]
	v_add_f32_e32 v66, 1.0, v66
	v_exp_f32_e32 v74, v74
	v_add_f32_e32 v67, 1.0, v67
	v_exp_f32_e32 v75, v75
	v_add_f32_e32 v68, 1.0, v68
	v_exp_f32_e32 v76, v76
	v_add_f32_e32 v69, 1.0, v69
	v_exp_f32_e32 v77, v77
	v_rcp_f32_e32 v66, v66
	v_add_f32_e32 v74, 1.0, v74
	v_rcp_f32_e32 v67, v67
	v_add_f32_e32 v75, 1.0, v75
	v_rcp_f32_e32 v68, v68
	v_add_f32_e32 v76, 1.0, v76
	v_rcp_f32_e32 v69, v69
	v_add_f32_e32 v77, 1.0, v77
	v_pk_mul_f32 v[66:67], v[14:15], v[66:67]
	v_rcp_f32_e32 v74, v74
	v_pk_mul_f32 v[68:69], v[16:17], v[68:69]
	v_rcp_f32_e32 v75, v75
	v_pk_mul_f32 v[66:67], v[10:11], v[66:67]
	v_rcp_f32_e32 v76, v76
	v_pk_mul_f32 v[68:69], v[12:13], v[68:69]
	v_rcp_f32_e32 v77, v77
	v_pk_mul_f32 v[74:75], v[6:7], v[74:75]
	v_pk_mul_f32 v[74:75], v[2:3], v[74:75]
	v_pk_mul_f32 v[76:77], v[8:9], v[76:77]
	v_pk_mul_f32 v[76:77], v[4:5], v[76:77]
	v_cvt_pk_fp8_f32 v10, v66, v67
	v_cvt_pk_fp8_f32 v10, v68, v69 op_sel:[0,0,1]
	v_cvt_pk_fp8_f32 v11, v74, v75
	v_cvt_pk_fp8_f32 v11, v76, v77 op_sel:[0,0,1]
	v_mad_i64_i32 v[2:3], s[18:19], v0, s78, v[132:133]
	v_lshl_add_u64 v[2:3], v[2:3], 0, v[130:131]
	s_mov_b64 s[18:19], -1
	global_store_dwordx2 v[2:3], v[10:11], off
	s_cbranch_vccnz .LBB0_1837
	s_and_b64 vcc, exec, s[38:39]
	s_cbranch_vccnz .LBB0_1836
	s_barrier
	s_branch .LBB0_1836
